# MLA attention: softmax row sums moved off the matrix core (ones x P MFMAs replaced by per-lane v_dot2c_f32_bf16 sums of the same bf16 P values, lane halves combined once at the end): 1/6 fewer MFMAs i
# speedup vs baseline: 1.0047x; 1.0047x over previous
.LBB0_1539:
	v_exp_f32_e32 v36, v116
	v_exp_f32_e32 v40, v132
	v_exp_f32_e32 v37, v117
	v_exp_f32_e32 v41, v133
	v_exp_f32_e32 v38, v118
	v_exp_f32_e32 v42, v134
	v_exp_f32_e32 v39, v119
	v_exp_f32_e32 v43, v135
	v_exp_f32_e32 v44, v120
	v_exp_f32_e32 v45, v136
	v_exp_f32_e32 v46, v121
	v_exp_f32_e32 v47, v137
	v_exp_f32_e32 v48, v122
	v_exp_f32_e32 v49, v138
	v_exp_f32_e32 v50, v123
	v_exp_f32_e32 v51, v139
	v_exp_f32_e32 v52, v124
	v_exp_f32_e32 v53, v140
	v_exp_f32_e32 v54, v125
	v_exp_f32_e32 v55, v141
	v_exp_f32_e32 v56, v126
	v_exp_f32_e32 v57, v142
	v_exp_f32_e32 v58, v127
	v_exp_f32_e32 v59, v143
	v_exp_f32_e32 v60, v128
	v_exp_f32_e32 v61, v144
	v_exp_f32_e32 v62, v129
	v_exp_f32_e32 v63, v145
	v_exp_f32_e32 v64, v130
	v_exp_f32_e32 v65, v146
	v_exp_f32_e32 v66, v131
	v_exp_f32_e32 v68, v147
	v_cvt_pk_bf16_f32 v36, v36, v37
	v_cvt_pk_bf16_f32 v37, v38, v39
	v_cvt_pk_bf16_f32 v38, v44, v46
	v_cvt_pk_bf16_f32 v39, v48, v50
	v_cvt_pk_bf16_f32 v40, v40, v41
	v_cvt_pk_bf16_f32 v41, v42, v43
	v_cvt_pk_bf16_f32 v42, v45, v47
	v_cvt_pk_bf16_f32 v43, v49, v51
	v_cvt_pk_bf16_f32 v44, v52, v54
	v_cvt_pk_bf16_f32 v45, v56, v58
	v_cvt_pk_bf16_f32 v46, v60, v62
	v_cvt_pk_bf16_f32 v47, v64, v66
	v_cvt_pk_bf16_f32 v48, v53, v55
	v_cvt_pk_bf16_f32 v49, v57, v59
	v_cvt_pk_bf16_f32 v50, v61, v63
	v_cvt_pk_bf16_f32 v51, v65, v68
	v_mov_b64_e32 v[52:53], s[92:93]
	v_mov_b64_e32 v[54:55], s[94:95]
	ds_read_b64_tr_b16 v[56:57], v205 offset:0
	ds_read_b64_tr_b16 v[58:59], v205 offset:1024
	ds_read_b64_tr_b16 v[60:61], v67 offset:0
	ds_read_b64_tr_b16 v[62:63], v67 offset:1024
	s_nop 1
	v_dot2c_f32_bf16 v100, 0x3f803f80, v36
	v_dot2c_f32_bf16 v101, 0x3f803f80, v37
	v_dot2c_f32_bf16 v100, 0x3f803f80, v38
	v_dot2c_f32_bf16 v101, 0x3f803f80, v39
	v_dot2c_f32_bf16 v100, 0x3f803f80, v44
	v_dot2c_f32_bf16 v101, 0x3f803f80, v45
	v_dot2c_f32_bf16 v100, 0x3f803f80, v46
	v_dot2c_f32_bf16 v101, 0x3f803f80, v47
	v_dot2c_f32_bf16 v100, 0x3f803f80, v40
	v_dot2c_f32_bf16 v101, 0x3f803f80, v41
	v_dot2c_f32_bf16 v100, 0x3f803f80, v42
	v_dot2c_f32_bf16 v101, 0x3f803f80, v43
	v_dot2c_f32_bf16 v100, 0x3f803f80, v48
	v_dot2c_f32_bf16 v101, 0x3f803f80, v49
	v_dot2c_f32_bf16 v100, 0x3f803f80, v50
	v_dot2c_f32_bf16 v101, 0x3f803f80, v51
	ds_read_b64_tr_b16 v[52:53], v205 offset:2048
	ds_read_b64_tr_b16 v[54:55], v205 offset:3072
	ds_read_b64_tr_b16 v[68:69], v67 offset:2048
	ds_read_b64_tr_b16 v[70:71], v67 offset:3072
	s_nop 0
	s_waitcnt lgkmcnt(0)
	s_nop 0
	v_mfma_f32_32x32x16_bf16 v[2:17], v[56:59], v[36:39], v[2:17]
	v_mfma_f32_32x32x16_bf16 v[18:33], v[60:63], v[36:39], v[18:33]
	ds_read_b64_tr_b16 v[36:37], v205 offset:4096
	ds_read_b64_tr_b16 v[38:39], v205 offset:5120
	v_mfma_f32_32x32x16_bf16 v[2:17], v[52:55], v[44:47], v[2:17]
	v_mfma_f32_32x32x16_bf16 v[18:33], v[68:71], v[44:47], v[18:33]
	ds_read_b64_tr_b16 v[44:45], v67 offset:4096
	ds_read_b64_tr_b16 v[46:47], v67 offset:5120
	ds_read_b64_tr_b16 v[52:53], v205 offset:6144
	ds_read_b64_tr_b16 v[54:55], v205 offset:7168
	ds_read_b64_tr_b16 v[56:57], v67 offset:6144
	ds_read_b64_tr_b16 v[58:59], v67 offset:7168
	s_nop 0
	s_waitcnt lgkmcnt(0)
	s_nop 0
	v_mfma_f32_32x32x16_bf16 v[2:17], v[36:39], v[40:43], v[2:17]
	v_mfma_f32_32x32x16_bf16 v[18:33], v[44:47], v[40:43], v[18:33]
	v_mfma_f32_32x32x16_bf16 v[2:17], v[52:55], v[48:51], v[2:17]
	v_mfma_f32_32x32x16_bf16 v[18:33], v[56:59], v[48:51], v[18:33]
	s_setprio 0
	v_add_f32_e32 v34, v100, v101
	v_mov_b32_e32 v38, v34
	s_nop 1
	v_permlane32_swap_b32_e32 v34, v38
	v_add_f32_e32 v34, v34, v38
	v_div_scale_f32 v38, s[2:3], v34, v34, 1.0
	v_rcp_f32_e32 v39, v38
	v_lshlrev_b64 v[36:37], 11, v[172:173]
	v_lshl_add_u64 v[36:37], s[52:53], 0, v[36:37]
	s_lshl_b32 s4, s12, 1
	v_fma_f32 v40, -v38, v39, 1.0
	v_fmac_f32_e32 v39, v40, v39
	v_div_scale_f32 v40, vcc, 1.0, v34, 1.0
	v_mul_f32_e32 v41, v40, v39
	v_fma_f32 v42, -v38, v41, v40
	v_fmac_f32_e32 v41, v42, v39
	v_fma_f32 v38, -v38, v41, v40
	v_div_fmas_f32 v38, v38, v39, v41
	v_div_fixup_f32 v34, v38, v34, 1.0
	v_pk_mul_f32 v[2:3], v[2:3], v[34:35] op_sel_hi:[1,0]
	v_pk_mul_f32 v[4:5], v[4:5], v[34:35] op_sel_hi:[1,0]
	v_cvt_pk_bf16_f32 v2, v2, v3
	v_cvt_pk_bf16_f32 v3, v4, v5
	v_pk_mul_f32 v[4:5], v[6:7], v[34:35] op_sel_hi:[1,0]
	v_pk_mul_f32 v[6:7], v[8:9], v[34:35] op_sel_hi:[1,0]
	v_lshl_add_u64 v[36:37], v[36:37], 0, s[4:5]
	v_lshlrev_b32_e32 v98, 1, v35
	v_cvt_pk_bf16_f32 v4, v4, v5
	v_cvt_pk_bf16_f32 v5, v6, v7
	v_lshl_add_u64 v[36:37], v[36:37], 0, v[98:99]
	v_permlane32_swap_b32_e32 v2, v4
	v_permlane32_swap_b32_e32 v3, v5
	global_store_dwordx4 v[36:37], v[2:5], off
	v_pk_mul_f32 v[6:7], v[16:17], v[34:35] op_sel_hi:[1,0]
	s_addk_i32 s87, 0x100
	v_pk_mul_f32 v[2:3], v[10:11], v[34:35] op_sel_hi:[1,0]
	v_pk_mul_f32 v[4:5], v[12:13], v[34:35] op_sel_hi:[1,0]
	v_cvt_pk_bf16_f32 v2, v2, v3
	v_cvt_pk_bf16_f32 v3, v4, v5
	v_pk_mul_f32 v[4:5], v[14:15], v[34:35] op_sel_hi:[1,0]
	s_cmp_ge_u32 s87, s86
	v_cvt_pk_bf16_f32 v4, v4, v5
	v_cvt_pk_bf16_f32 v5, v6, v7
	s_nop 0
	v_permlane32_swap_b32_e32 v2, v4
	v_permlane32_swap_b32_e32 v3, v5
	global_store_dwordx4 v[36:37], v[2:5], off offset:32
	v_pk_mul_f32 v[6:7], v[24:25], v[34:35] op_sel_hi:[1,0]
	s_nop 0
	v_pk_mul_f32 v[2:3], v[18:19], v[34:35] op_sel_hi:[1,0]
	v_pk_mul_f32 v[4:5], v[20:21], v[34:35] op_sel_hi:[1,0]
	v_cvt_pk_bf16_f32 v2, v2, v3
	v_cvt_pk_bf16_f32 v3, v4, v5
	v_pk_mul_f32 v[4:5], v[22:23], v[34:35] op_sel_hi:[1,0]
	s_nop 0
	v_cvt_pk_bf16_f32 v4, v4, v5
	v_cvt_pk_bf16_f32 v5, v6, v7
	s_nop 0
	v_permlane32_swap_b32_e32 v2, v4
	v_permlane32_swap_b32_e32 v3, v5
	global_store_dwordx4 v[36:37], v[2:5], off offset:64
	v_pk_mul_f32 v[6:7], v[32:33], v[34:35] op_sel_hi:[1,0]
	s_nop 0
	v_pk_mul_f32 v[2:3], v[26:27], v[34:35] op_sel_hi:[1,0]
	v_pk_mul_f32 v[4:5], v[28:29], v[34:35] op_sel_hi:[1,0]
	v_cvt_pk_bf16_f32 v2, v2, v3
	v_cvt_pk_bf16_f32 v3, v4, v5
	v_pk_mul_f32 v[4:5], v[30:31], v[34:35] op_sel_hi:[1,0]
	s_nop 0
	v_cvt_pk_bf16_f32 v4, v4, v5
	v_cvt_pk_bf16_f32 v5, v6, v7
	s_nop 0
	v_permlane32_swap_b32_e32 v2, v4
	v_permlane32_swap_b32_e32 v3, v5
	global_store_dwordx4 v[36:37], v[2:5], off offset:96
	s_cbranch_scc1 .LBB0_1679

.LBB0_1598:
	ds_read_b128 v[36:39], v211 offset:12288
	ds_read_b128 v[52:55], v211 offset:12320
	ds_read_b128 v[56:59], v211 offset:18432
	ds_read_b128 v[60:63], v211 offset:18464
	v_exp_f32_e32 v84, v116
	v_exp_f32_e32 v98, v132
	s_waitcnt lgkmcnt(0)
	v_mfma_f32_32x32x16_bf16 v[36:51], v[36:39], v[168:171], 0
	v_exp_f32_e32 v85, v117
	v_exp_f32_e32 v116, v133
	v_exp_f32_e32 v117, v118
	v_exp_f32_e32 v118, v134
	v_exp_f32_e32 v125, v125
	v_exp_f32_e32 v132, v141
	v_exp_f32_e32 v129, v129
	v_mfma_f32_32x32x16_bf16 v[68:83], v[56:59], v[168:171], 0
	v_cvt_pk_bf16_f32 v84, v84, v85
	v_mfma_f32_32x32x16_bf16 v[36:51], v[52:55], v[148:151], v[36:51]
	ds_read_b128 v[52:55], v211 offset:12352
	ds_read_b128 v[56:59], v211 offset:12384
	v_mfma_f32_32x32x16_bf16 v[68:83], v[60:63], v[148:151], v[68:83]
	v_exp_f32_e32 v61, v126
	v_exp_f32_e32 v126, v142
	v_exp_f32_e32 v62, v127
	v_exp_f32_e32 v127, v143
	v_exp_f32_e32 v63, v128
	v_exp_f32_e32 v128, v144
	v_cvt_pk_bf16_f32 v61, v61, v62
	s_waitcnt lgkmcnt(0)
	v_mfma_f32_32x32x16_bf16 v[36:51], v[52:55], v[152:155], v[36:51]
	ds_read_b128 v[52:55], v211 offset:18496
	ds_read_b128 v[86:89], v211 offset:18528
	ds_read_b128 v[90:93], v226 offset:12288
	ds_read_b128 v[94:97], v226 offset:18432
	v_cvt_pk_bf16_f32 v62, v63, v129
	s_waitcnt lgkmcnt(0)
	v_mfma_f32_32x32x16_bf16 v[68:83], v[52:55], v[152:155], v[68:83]
	v_exp_f32_e32 v54, v145
	v_exp_f32_e32 v52, v130
	v_exp_f32_e32 v55, v146
	v_exp_f32_e32 v53, v131
	v_exp_f32_e32 v130, v147
	v_cvt_pk_bf16_f32 v54, v128, v54
	v_cvt_pk_bf16_f32 v63, v52, v53
	v_mfma_f32_32x32x16_bf16 v[36:51], v[56:59], v[156:159], v[36:51]
	ds_read_b128 v[56:59], v227 offset:12288
	ds_read_b128 v[236:239], v227 offset:18432
	v_cvt_pk_bf16_f32 v53, v126, v127
	v_cvt_pk_bf16_f32 v55, v55, v130
	v_mfma_f32_32x32x16_bf16 v[68:83], v[86:89], v[156:159], v[68:83]
	v_mfma_f32_32x32x16_bf16 v[36:51], v[90:93], v[160:163], v[36:51]
	v_exp_f32_e32 v90, v119
	v_exp_f32_e32 v91, v135
	v_exp_f32_e32 v92, v120
	v_exp_f32_e32 v93, v136
	v_exp_f32_e32 v119, v121
	v_exp_f32_e32 v120, v137
	v_exp_f32_e32 v121, v122
	v_mfma_f32_32x32x16_bf16 v[68:83], v[94:97], v[160:163], v[68:83]
	v_exp_f32_e32 v122, v139
	v_cvt_pk_bf16_f32 v85, v117, v90
	v_cvt_pk_bf16_f32 v86, v92, v119
	s_waitcnt lgkmcnt(0)
	v_mfma_f32_32x32x16_bf16 v[36:51], v[56:59], v[164:167], v[36:51]
	v_exp_f32_e32 v59, v138
	v_exp_f32_e32 v56, v123
	v_exp_f32_e32 v123, v124
	v_exp_f32_e32 v124, v140
	v_cvt_pk_bf16_f32 v57, v118, v91
	v_cvt_pk_bf16_f32 v87, v121, v56
	v_cvt_pk_bf16_f32 v56, v98, v116
	v_mfma_f32_32x32x16_bf16 v[68:83], v[236:239], v[164:167], v[68:83]
	v_cvt_pk_bf16_f32 v58, v93, v120
	v_cvt_pk_bf16_f32 v59, v59, v122
	v_cvt_pk_bf16_f32 v60, v123, v125
	v_cvt_pk_bf16_f32 v52, v124, v132
	v_max3_f32 v96, v36, v37, v68
	v_max_f32_e32 v97, v51, v51
	v_max3_f32 v96, v96, v69, v38
	ds_read_b64_tr_b16 v[120:121], v234 offset:0
	ds_read_b64_tr_b16 v[122:123], v234 offset:1024
	s_nop 0
	v_dot2c_f32_bf16 v100, 0x3f803f80, v84
	v_dot2c_f32_bf16 v101, 0x3f803f80, v85
	v_dot2c_f32_bf16 v100, 0x3f803f80, v86
	v_dot2c_f32_bf16 v101, 0x3f803f80, v87
	v_max3_f32 v96, v96, v70, v71
	ds_read_b64_tr_b16 v[116:117], v235 offset:0
	ds_read_b64_tr_b16 v[118:119], v235 offset:1024
	ds_read_b64_tr_b16 v[92:93], v234 offset:2048
	ds_read_b64_tr_b16 v[94:95], v234 offset:3072
	ds_read_b64_tr_b16 v[88:89], v235 offset:2048
	s_nop 0
	v_max3_f32 v96, v96, v39, v40
	v_dot2c_f32_bf16 v100, 0x3f803f80, v60
	v_dot2c_f32_bf16 v101, 0x3f803f80, v61
	v_dot2c_f32_bf16 v100, 0x3f803f80, v62
	v_dot2c_f32_bf16 v101, 0x3f803f80, v63
	v_max3_f32 v96, v96, v72, v73
	ds_read_b64_tr_b16 v[90:91], v235 offset:3072
	s_nop 0
	v_max3_f32 v96, v96, v41, v42
	v_max3_f32 v96, v96, v74, v75
	v_max3_f32 v96, v96, v43, v44
	v_dot2c_f32_bf16 v100, 0x3f803f80, v56
	v_dot2c_f32_bf16 v101, 0x3f803f80, v57
	v_dot2c_f32_bf16 v100, 0x3f803f80, v58
	v_dot2c_f32_bf16 v101, 0x3f803f80, v59
	v_max3_f32 v96, v96, v76, v77
	v_max3_f32 v96, v96, v45, v46
	v_max3_f32 v96, v96, v78, v79
	v_max3_f32 v96, v96, v47, v48
	v_dot2c_f32_bf16 v100, 0x3f803f80, v52
	v_dot2c_f32_bf16 v101, 0x3f803f80, v53
	v_dot2c_f32_bf16 v100, 0x3f803f80, v54
	v_dot2c_f32_bf16 v101, 0x3f803f80, v55
	v_max3_f32 v96, v96, v80, v81
	v_max3_f32 v96, v96, v49, v50
	v_max3_f32 v96, v96, v82, v83
	v_max_f32_e32 v96, v96, v96
	v_max_f32_e32 v96, v96, v97
	v_mov_b32_e32 v97, v96
	s_nop 1
	v_permlane32_swap_b32_e32 v96, v97
	v_sub_f32_e32 v96, v96, v66
	s_waitcnt lgkmcnt(0)
	s_nop 0
	v_mfma_f32_32x32x16_bf16 v[2:17], v[120:123], v[84:87], v[2:17]
	v_mfma_f32_32x32x16_bf16 v[18:33], v[116:119], v[84:87], v[18:33]
	v_mfma_f32_32x32x16_bf16 v[2:17], v[92:95], v[60:63], v[2:17]
	v_mfma_f32_32x32x16_bf16 v[18:33], v[88:91], v[60:63], v[18:33]
	ds_read_b64_tr_b16 v[60:61], v234 offset:4096
	ds_read_b64_tr_b16 v[62:63], v234 offset:5120
	ds_read_b64_tr_b16 v[84:85], v235 offset:4096
	ds_read_b64_tr_b16 v[86:87], v235 offset:5120
	ds_read_b64_tr_b16 v[88:89], v234 offset:6144
	ds_read_b64_tr_b16 v[90:91], v234 offset:7168
	ds_read_b64_tr_b16 v[92:93], v235 offset:6144
	ds_read_b64_tr_b16 v[94:95], v235 offset:7168
	s_nop 0
	s_waitcnt lgkmcnt(0)
	s_nop 0
	v_mfma_f32_32x32x16_bf16 v[2:17], v[60:63], v[56:59], v[2:17]
	v_mfma_f32_32x32x16_bf16 v[18:33], v[84:87], v[56:59], v[18:33]
	v_mfma_f32_32x32x16_bf16 v[2:17], v[88:91], v[52:55], v[2:17]
	v_mfma_f32_32x32x16_bf16 v[18:33], v[92:95], v[52:55], v[18:33]
	v_cmp_lt_f32_e32 vcc, s29, v96
	s_cbranch_vccz .LBB0_1600
	v_max_f32_e32 v52, v96, v96
	v_max_f32_e32 v53, 0, v52
	v_exp_f32_e64 v52, -v53
	v_add_f32_e32 v66, v66, v53
	v_mul_f32_e32 v34, v34, v52
	v_pk_mul_f32 v[114:115], v[114:115], v[52:53] op_sel_hi:[1,0]
	v_pk_mul_f32 v[112:113], v[112:113], v[52:53] op_sel_hi:[1,0]
	v_pk_mul_f32 v[110:111], v[110:111], v[52:53] op_sel_hi:[1,0]
	v_pk_mul_f32 v[108:109], v[108:109], v[52:53] op_sel_hi:[1,0]
	v_pk_mul_f32 v[106:107], v[106:107], v[52:53] op_sel_hi:[1,0]
	v_pk_mul_f32 v[104:105], v[104:105], v[52:53] op_sel_hi:[1,0]
	v_pk_mul_f32 v[102:103], v[102:103], v[52:53] op_sel_hi:[1,0]
	v_pk_mul_f32 v[100:101], v[100:101], v[52:53] op_sel_hi:[1,0]
	v_pk_mul_f32 v[32:33], v[52:53], v[32:33] op_sel_hi:[0,1]
	v_pk_mul_f32 v[30:31], v[52:53], v[30:31] op_sel_hi:[0,1]
	v_pk_mul_f32 v[28:29], v[52:53], v[28:29] op_sel_hi:[0,1]
	v_pk_mul_f32 v[26:27], v[52:53], v[26:27] op_sel_hi:[0,1]
	v_pk_mul_f32 v[24:25], v[52:53], v[24:25] op_sel_hi:[0,1]
	v_pk_mul_f32 v[22:23], v[52:53], v[22:23] op_sel_hi:[0,1]
	v_pk_mul_f32 v[20:21], v[52:53], v[20:21] op_sel_hi:[0,1]
	v_pk_mul_f32 v[18:19], v[52:53], v[18:19] op_sel_hi:[0,1]
	v_pk_mul_f32 v[16:17], v[52:53], v[16:17] op_sel_hi:[0,1]
	v_pk_mul_f32 v[14:15], v[52:53], v[14:15] op_sel_hi:[0,1]
	v_pk_mul_f32 v[12:13], v[52:53], v[12:13] op_sel_hi:[0,1]
	v_pk_mul_f32 v[10:11], v[52:53], v[10:11] op_sel_hi:[0,1]
	v_pk_mul_f32 v[8:9], v[52:53], v[8:9] op_sel_hi:[0,1]
	v_pk_mul_f32 v[6:7], v[52:53], v[6:7] op_sel_hi:[0,1]
	v_pk_mul_f32 v[4:5], v[52:53], v[4:5] op_sel_hi:[0,1]
	v_pk_mul_f32 v[2:3], v[52:53], v[2:3] op_sel_hi:[0,1]

.LBB0_1631:
	s_mov_b32 s31, s89
	ds_read_b128 v[52:55], v211
	ds_read_b128 v[56:59], v211 offset:32
	v_exp_f32_e32 v36, v36
	v_exp_f32_e32 v68, v68
	v_exp_f32_e32 v37, v37
	s_waitcnt lgkmcnt(0)
	v_mfma_f32_32x32x16_bf16 v[116:131], v[52:55], v[168:171], 0
	ds_read_b128 v[52:55], v211 offset:6144
	ds_read_b128 v[60:63], v211 offset:6176
	v_exp_f32_e32 v69, v69
	v_exp_f32_e32 v38, v38
	v_exp_f32_e32 v70, v70
	v_exp_f32_e32 v39, v39
	v_exp_f32_e32 v71, v71
	v_exp_f32_e32 v40, v40
	s_waitcnt lgkmcnt(0)
	v_mfma_f32_32x32x16_bf16 v[132:147], v[52:55], v[168:171], 0
	v_exp_f32_e32 v72, v72
	v_exp_f32_e32 v41, v41
	v_exp_f32_e32 v73, v73
	v_exp_f32_e32 v42, v42
	v_exp_f32_e32 v43, v43
	v_exp_f32_e32 v44, v44
	v_exp_f32_e32 v45, v45
	v_mfma_f32_32x32x16_bf16 v[116:131], v[56:59], v[148:151], v[116:131]
	ds_read_b128 v[52:55], v211 offset:64
	ds_read_b128 v[56:59], v211 offset:96
	v_exp_f32_e32 v46, v46
	v_exp_f32_e32 v47, v47
	v_cvt_pk_bf16_f32 v44, v44, v45
	v_cvt_pk_bf16_f32 v45, v46, v47
	v_mfma_f32_32x32x16_bf16 v[132:147], v[60:63], v[148:151], v[132:147]
	v_exp_f32_e32 v60, v78
	v_exp_f32_e32 v61, v79
	v_exp_f32_e32 v62, v48
	v_exp_f32_e32 v63, v80
	v_cvt_pk_bf16_f32 v48, v36, v37
	v_cvt_pk_bf16_f32 v37, v60, v61
	s_waitcnt lgkmcnt(0)
	v_mfma_f32_32x32x16_bf16 v[116:131], v[52:55], v[152:155], v[116:131]
	ds_read_b128 v[52:55], v211 offset:6208
	ds_read_b128 v[84:87], v211 offset:6240
	ds_read_b128 v[88:91], v226
	ds_read_b128 v[92:95], v226 offset:6144
	s_waitcnt lgkmcnt(0)
	v_mfma_f32_32x32x16_bf16 v[132:147], v[52:55], v[152:155], v[132:147]
	v_exp_f32_e32 v52, v81
	v_exp_f32_e32 v53, v50
	v_exp_f32_e32 v54, v82
	v_exp_f32_e32 v55, v51
	v_cvt_pk_bf16_f32 v50, v40, v41
	v_cvt_pk_bf16_f32 v51, v42, v43
	v_cvt_pk_bf16_f32 v40, v68, v69
	v_mfma_f32_32x32x16_bf16 v[116:131], v[56:59], v[156:159], v[116:131]
	ds_read_b128 v[56:59], v227
	ds_read_b128 v[236:239], v227 offset:6144
	v_cvt_pk_bf16_f32 v41, v70, v71
	v_cvt_pk_bf16_f32 v42, v72, v73
	v_cvt_pk_bf16_f32 v47, v53, v55
	v_mfma_f32_32x32x16_bf16 v[132:147], v[84:87], v[156:159], v[132:147]
	v_mfma_f32_32x32x16_bf16 v[116:131], v[88:91], v[160:163], v[116:131]
	v_mfma_f32_32x32x16_bf16 v[132:147], v[92:95], v[160:163], v[132:147]
	s_waitcnt lgkmcnt(0)
	v_mfma_f32_32x32x16_bf16 v[116:131], v[56:59], v[164:167], v[116:131]
	v_exp_f32_e32 v56, v74
	v_exp_f32_e32 v57, v75
	v_exp_f32_e32 v58, v76
	v_exp_f32_e32 v59, v77
	v_exp_f32_e32 v74, v49
	v_exp_f32_e32 v75, v83
	v_cvt_pk_bf16_f32 v49, v38, v39
	v_mfma_f32_32x32x16_bf16 v[132:147], v[236:239], v[164:167], v[132:147]
	v_cvt_pk_bf16_f32 v43, v56, v57
	v_cvt_pk_bf16_f32 v46, v62, v74
	v_cvt_pk_bf16_f32 v36, v58, v59
	v_cvt_pk_bf16_f32 v38, v63, v52
	v_cvt_pk_bf16_f32 v39, v54, v75
	v_max3_f32 v72, v116, v117, v132
	v_max_f32_e32 v73, v131, v131
	v_max3_f32 v72, v72, v133, v118
	ds_read_b64_tr_b16 v[68:69], v205 offset:0
	ds_read_b64_tr_b16 v[70:71], v205 offset:1024
	s_nop 0
	v_dot2c_f32_bf16 v100, 0x3f803f80, v48
	v_dot2c_f32_bf16 v101, 0x3f803f80, v49
	v_dot2c_f32_bf16 v100, 0x3f803f80, v50
	v_dot2c_f32_bf16 v101, 0x3f803f80, v51
	v_max3_f32 v72, v72, v134, v135
	ds_read_b64_tr_b16 v[60:61], v67 offset:0
	ds_read_b64_tr_b16 v[62:63], v67 offset:1024
	ds_read_b64_tr_b16 v[56:57], v205 offset:2048
	ds_read_b64_tr_b16 v[58:59], v205 offset:3072
	ds_read_b64_tr_b16 v[52:53], v67 offset:2048
	s_nop 0
	v_max3_f32 v72, v72, v119, v120
	v_dot2c_f32_bf16 v100, 0x3f803f80, v44
	v_dot2c_f32_bf16 v101, 0x3f803f80, v45
	v_dot2c_f32_bf16 v100, 0x3f803f80, v46
	v_dot2c_f32_bf16 v101, 0x3f803f80, v47
	v_max3_f32 v72, v72, v136, v137
	ds_read_b64_tr_b16 v[54:55], v67 offset:3072
	s_nop 0
	v_max3_f32 v72, v72, v121, v122
	v_max3_f32 v72, v72, v138, v139
	v_max3_f32 v72, v72, v123, v124
	v_dot2c_f32_bf16 v100, 0x3f803f80, v40
	v_dot2c_f32_bf16 v101, 0x3f803f80, v41
	v_dot2c_f32_bf16 v100, 0x3f803f80, v42
	v_dot2c_f32_bf16 v101, 0x3f803f80, v43
	v_max3_f32 v72, v72, v140, v141
	v_max3_f32 v72, v72, v125, v126
	v_max3_f32 v72, v72, v142, v143
	v_max3_f32 v72, v72, v127, v128
	v_dot2c_f32_bf16 v100, 0x3f803f80, v36
	v_dot2c_f32_bf16 v101, 0x3f803f80, v37
	v_dot2c_f32_bf16 v100, 0x3f803f80, v38
	v_dot2c_f32_bf16 v101, 0x3f803f80, v39
	v_max3_f32 v72, v72, v144, v145
	v_max3_f32 v72, v72, v129, v130
	v_max3_f32 v72, v72, v146, v147
	v_max_f32_e32 v72, v72, v72
	v_max_f32_e32 v72, v72, v73
	v_mov_b32_e32 v73, v72
	s_nop 1
	v_permlane32_swap_b32_e32 v72, v73
	v_sub_f32_e32 v72, v72, v66
	s_waitcnt lgkmcnt(0)
	s_nop 0
	v_mfma_f32_32x32x16_bf16 v[2:17], v[68:71], v[48:51], v[2:17]
	v_mfma_f32_32x32x16_bf16 v[18:33], v[60:63], v[48:51], v[18:33]
	v_mfma_f32_32x32x16_bf16 v[2:17], v[56:59], v[44:47], v[2:17]
	v_mfma_f32_32x32x16_bf16 v[18:33], v[52:55], v[44:47], v[18:33]
	ds_read_b64_tr_b16 v[44:45], v205 offset:4096
	ds_read_b64_tr_b16 v[46:47], v205 offset:5120
	ds_read_b64_tr_b16 v[48:49], v67 offset:4096
	ds_read_b64_tr_b16 v[50:51], v67 offset:5120
	ds_read_b64_tr_b16 v[52:53], v205 offset:6144
	ds_read_b64_tr_b16 v[54:55], v205 offset:7168
	ds_read_b64_tr_b16 v[56:57], v67 offset:6144
	ds_read_b64_tr_b16 v[58:59], v67 offset:7168
	s_nop 0
	s_waitcnt lgkmcnt(0)
	s_nop 0
	v_mfma_f32_32x32x16_bf16 v[2:17], v[44:47], v[40:43], v[2:17]
	v_mfma_f32_32x32x16_bf16 v[18:33], v[48:51], v[40:43], v[18:33]
	v_mfma_f32_32x32x16_bf16 v[2:17], v[52:55], v[36:39], v[2:17]
	v_mfma_f32_32x32x16_bf16 v[18:33], v[56:59], v[36:39], v[18:33]
	v_cmp_lt_f32_e32 vcc, s29, v72
	s_cbranch_vccz .LBB0_1633
	v_max_f32_e32 v36, v72, v72
	v_max_f32_e32 v37, 0, v36
	v_exp_f32_e64 v36, -v37
	v_add_f32_e32 v66, v66, v37
	v_mul_f32_e32 v34, v34, v36
	v_pk_mul_f32 v[114:115], v[114:115], v[36:37] op_sel_hi:[1,0]
	v_pk_mul_f32 v[112:113], v[112:113], v[36:37] op_sel_hi:[1,0]
	v_pk_mul_f32 v[110:111], v[110:111], v[36:37] op_sel_hi:[1,0]
	v_pk_mul_f32 v[108:109], v[108:109], v[36:37] op_sel_hi:[1,0]
	v_pk_mul_f32 v[106:107], v[106:107], v[36:37] op_sel_hi:[1,0]
	v_pk_mul_f32 v[104:105], v[104:105], v[36:37] op_sel_hi:[1,0]
	v_pk_mul_f32 v[102:103], v[102:103], v[36:37] op_sel_hi:[1,0]
	v_pk_mul_f32 v[100:101], v[100:101], v[36:37] op_sel_hi:[1,0]
	v_pk_mul_f32 v[32:33], v[36:37], v[32:33] op_sel_hi:[0,1]
	v_pk_mul_f32 v[30:31], v[36:37], v[30:31] op_sel_hi:[0,1]
	v_pk_mul_f32 v[28:29], v[36:37], v[28:29] op_sel_hi:[0,1]
	v_pk_mul_f32 v[26:27], v[36:37], v[26:27] op_sel_hi:[0,1]
	v_pk_mul_f32 v[24:25], v[36:37], v[24:25] op_sel_hi:[0,1]
	v_pk_mul_f32 v[22:23], v[36:37], v[22:23] op_sel_hi:[0,1]
	v_pk_mul_f32 v[20:21], v[36:37], v[20:21] op_sel_hi:[0,1]
	v_pk_mul_f32 v[18:19], v[36:37], v[18:19] op_sel_hi:[0,1]
	v_pk_mul_f32 v[16:17], v[36:37], v[16:17] op_sel_hi:[0,1]
	v_pk_mul_f32 v[14:15], v[36:37], v[14:15] op_sel_hi:[0,1]
	v_pk_mul_f32 v[12:13], v[36:37], v[12:13] op_sel_hi:[0,1]
	v_pk_mul_f32 v[10:11], v[36:37], v[10:11] op_sel_hi:[0,1]
	v_pk_mul_f32 v[8:9], v[36:37], v[8:9] op_sel_hi:[0,1]
	v_pk_mul_f32 v[6:7], v[36:37], v[6:7] op_sel_hi:[0,1]
	v_pk_mul_f32 v[4:5], v[36:37], v[4:5] op_sel_hi:[0,1]
	v_pk_mul_f32 v[2:3], v[36:37], v[2:3] op_sel_hi:[0,1]

.LBB0_1666:
	s_bitcmp1_b32 s11, 0
	s_cselect_b32 s4, 0x3000, 0
	s_add_i32 s4, s4, 0
	v_add_u32_e32 v92, s4, v207
	ds_read_b128 v[36:39], v92
	ds_read_b128 v[52:55], v92 offset:32
	v_add3_u32 v64, v207, v208, s4
	v_exp_f32_e32 v93, v116
	v_exp_f32_e32 v94, v117
	s_waitcnt lgkmcnt(0)
	v_mfma_f32_32x32x16_bf16 v[68:83], v[36:39], v[168:171], 0
	ds_read_b128 v[36:39], v92 offset:6144
	ds_read_b128 v[56:59], v92 offset:6176
	ds_read_b128 v[60:63], v92 offset:96
	v_exp_f32_e32 v95, v118
	v_exp_f32_e32 v96, v119
	v_exp_f32_e32 v97, v120
	v_exp_f32_e32 v98, v121
	v_add3_u32 v88, v207, v206, s4
	v_mfma_f32_32x32x16_bf16 v[68:83], v[52:55], v[148:151], v[68:83]
	ds_read_b128 v[52:55], v92 offset:64
	v_exp_f32_e32 v174, v128
	v_exp_f32_e32 v175, v129
	v_exp_f32_e32 v176, v130
	v_exp_f32_e32 v177, v131
	s_waitcnt lgkmcnt(0)
	v_mfma_f32_32x32x16_bf16 v[36:51], v[36:39], v[168:171], 0
	v_exp_f32_e32 v168, v122
	v_exp_f32_e32 v169, v125
	v_exp_f32_e32 v170, v126
	v_exp_f32_e32 v171, v127
	v_mfma_f32_32x32x16_bf16 v[68:83], v[52:55], v[152:155], v[68:83]
	ds_read_b128 v[52:55], v64
	v_mfma_f32_32x32x16_bf16 v[68:83], v[60:63], v[156:159], v[68:83]
	v_exp_f32_e32 v60, v123
	v_exp_f32_e32 v61, v124
	ds_read_b128 v[62:65], v64 offset:6144
	ds_read_b128 v[84:87], v88
	ds_read_b128 v[88:91], v88 offset:6144
	s_waitcnt lgkmcnt(0)
	v_mfma_f32_32x32x16_bf16 v[68:83], v[52:55], v[160:163], v[68:83]
	v_mfma_f32_32x32x16_bf16 v[36:51], v[56:59], v[148:151], v[36:51]
	s_nop 10
	v_mov_b64_e32 v[130:131], v[82:83]
	v_mov_b64_e32 v[128:129], v[80:81]
	v_mov_b64_e32 v[126:127], v[78:79]
	v_mov_b64_e32 v[124:125], v[76:77]
	v_mov_b64_e32 v[122:123], v[74:75]
	v_mov_b64_e32 v[120:121], v[72:73]
	v_mov_b64_e32 v[118:119], v[70:71]
	v_mov_b64_e32 v[116:117], v[68:69]
	ds_read_b128 v[52:55], v92 offset:6208
	ds_read_b128 v[72:75], v92 offset:6240
	s_waitcnt lgkmcnt(0)
	v_mfma_f32_32x32x16_bf16 v[36:51], v[52:55], v[152:155], v[36:51]
	v_exp_f32_e32 v76, v132
	v_exp_f32_e32 v77, v133
	v_exp_f32_e32 v78, v134
	v_exp_f32_e32 v79, v135
	v_exp_f32_e32 v80, v136
	v_exp_f32_e32 v58, v137
	v_exp_f32_e32 v59, v138
	v_mfma_f32_32x32x16_bf16 v[36:51], v[72:75], v[156:159], v[36:51]
	v_exp_f32_e32 v81, v139
	v_exp_f32_e32 v82, v140
	v_exp_f32_e32 v83, v141
	v_exp_f32_e32 v54, v144
	v_exp_f32_e32 v55, v145
	v_cvt_pk_bf16_f32 v68, v93, v94
	v_cvt_pk_bf16_f32 v69, v95, v96
	v_mfma_f32_32x32x16_bf16 v[36:51], v[62:65], v[160:163], v[36:51]
	v_cvt_pk_bf16_f32 v70, v97, v98
	v_cvt_pk_bf16_f32 v71, v168, v60
	v_cvt_pk_bf16_f32 v56, v76, v77
	v_cvt_pk_bf16_f32 v57, v78, v79
	v_cvt_pk_bf16_f32 v58, v80, v58
	v_cvt_pk_bf16_f32 v59, v59, v81
	v_cvt_pk_bf16_f32 v60, v61, v169
	v_mfma_f32_32x32x16_bf16 v[116:131], v[84:87], v[164:167], v[116:131]
	v_exp_f32_e32 v84, v142
	v_exp_f32_e32 v85, v143
	v_exp_f32_e32 v86, v146
	v_exp_f32_e32 v87, v147
	v_mov_b64_e32 v[146:147], v[50:51]
	v_mov_b64_e32 v[144:145], v[48:49]
	v_mov_b64_e32 v[142:143], v[46:47]
	v_mov_b64_e32 v[140:141], v[44:45]
	v_mov_b64_e32 v[138:139], v[42:43]
	v_mov_b64_e32 v[136:137], v[40:41]
	v_mov_b64_e32 v[134:135], v[38:39]
	v_mov_b64_e32 v[132:133], v[36:37]
	v_cvt_pk_bf16_f32 v61, v170, v171
	v_cvt_pk_bf16_f32 v62, v174, v175
	v_mfma_f32_32x32x16_bf16 v[132:147], v[88:91], v[164:167], v[132:147]
	v_cvt_pk_bf16_f32 v63, v176, v177
	v_cvt_pk_bf16_f32 v52, v82, v83
	v_cvt_pk_bf16_f32 v53, v84, v85
	v_cvt_pk_bf16_f32 v54, v54, v55
	v_cvt_pk_bf16_f32 v55, v86, v87
	v_mov_b64_e32 v[74:75], s[92:93]
	v_mov_b64_e32 v[76:77], s[94:95]
	v_max3_f32 v72, v116, v117, v132
	s_not_b32 s4, s11
	v_max3_f32 v72, v72, v133, v118
	s_lshl_b32 s4, s4, 13
	v_dot2c_f32_bf16 v100, 0x3f803f80, v68
	v_dot2c_f32_bf16 v101, 0x3f803f80, v69
	v_dot2c_f32_bf16 v100, 0x3f803f80, v70
	v_dot2c_f32_bf16 v101, 0x3f803f80, v71
	v_max3_f32 v72, v72, v134, v135
	v_max_f32_e32 v73, v131, v131
	v_max3_f32 v72, v72, v119, v120
	s_and_b32 s4, s4, 0x2000
	v_max3_f32 v72, v72, v136, v137
	s_add_i32 s4, s4, 0
	v_max3_f32 v72, v72, v121, v122
	v_dot2c_f32_bf16 v100, 0x3f803f80, v60
	v_dot2c_f32_bf16 v101, 0x3f803f80, v61
	v_dot2c_f32_bf16 v100, 0x3f803f80, v62
	v_dot2c_f32_bf16 v101, 0x3f803f80, v63
	v_max3_f32 v72, v72, v138, v139
	s_addk_i32 s4, 0x6000
	v_max3_f32 v72, v72, v123, v124
	v_add_u32_e32 v64, s4, v209
	v_max3_f32 v72, v72, v140, v141
	v_add_u32_e32 v65, s4, v210
	v_max3_f32 v72, v72, v125, v126
	v_dot2c_f32_bf16 v100, 0x3f803f80, v56
	v_dot2c_f32_bf16 v101, 0x3f803f80, v57
	v_dot2c_f32_bf16 v100, 0x3f803f80, v58
	v_dot2c_f32_bf16 v101, 0x3f803f80, v59
	v_max3_f32 v72, v72, v142, v143
	ds_read_b64_tr_b16 v[48:49], v64 offset:0
	ds_read_b64_tr_b16 v[50:51], v64 offset:1024
	ds_read_b64_tr_b16 v[44:45], v65 offset:0
	ds_read_b64_tr_b16 v[46:47], v65 offset:1024
	ds_read_b64_tr_b16 v[40:41], v64 offset:2048
	s_nop 0
	v_max3_f32 v72, v72, v127, v128
	ds_read_b64_tr_b16 v[42:43], v64 offset:3072
	ds_read_b64_tr_b16 v[36:37], v65 offset:2048
	ds_read_b64_tr_b16 v[38:39], v65 offset:3072
	v_dot2c_f32_bf16 v100, 0x3f803f80, v52
	v_dot2c_f32_bf16 v101, 0x3f803f80, v53
	v_dot2c_f32_bf16 v100, 0x3f803f80, v54
	v_dot2c_f32_bf16 v101, 0x3f803f80, v55
	v_max3_f32 v72, v72, v144, v145
	s_nop 0
	v_max3_f32 v72, v72, v129, v130
	s_nop 0
	v_max3_f32 v72, v72, v146, v147
	s_nop 0
	v_max_f32_e32 v72, v72, v72
	v_max_f32_e32 v72, v72, v73
	v_mov_b32_e32 v73, v72
	s_nop 1
	v_permlane32_swap_b32_e32 v72, v73
	v_sub_f32_e32 v72, v72, v66
	s_waitcnt lgkmcnt(0)
	s_nop 0
	v_mfma_f32_32x32x16_bf16 v[2:17], v[48:51], v[68:71], v[2:17]
	v_mfma_f32_32x32x16_bf16 v[18:33], v[44:47], v[68:71], v[18:33]
	v_mfma_f32_32x32x16_bf16 v[2:17], v[40:43], v[60:63], v[2:17]
	v_mfma_f32_32x32x16_bf16 v[18:33], v[36:39], v[60:63], v[18:33]
	ds_read_b64_tr_b16 v[36:37], v64 offset:4096
	ds_read_b64_tr_b16 v[38:39], v64 offset:5120
	ds_read_b64_tr_b16 v[40:41], v65 offset:4096
	ds_read_b64_tr_b16 v[42:43], v65 offset:5120
	ds_read_b64_tr_b16 v[44:45], v64 offset:6144
	ds_read_b64_tr_b16 v[46:47], v64 offset:7168
	ds_read_b64_tr_b16 v[48:49], v65 offset:6144
	ds_read_b64_tr_b16 v[50:51], v65 offset:7168
	s_nop 0
	s_waitcnt lgkmcnt(0)
	s_nop 0
	v_mfma_f32_32x32x16_bf16 v[2:17], v[36:39], v[56:59], v[2:17]
	v_mfma_f32_32x32x16_bf16 v[18:33], v[40:43], v[56:59], v[18:33]
	v_mfma_f32_32x32x16_bf16 v[2:17], v[44:47], v[52:55], v[2:17]
	v_mfma_f32_32x32x16_bf16 v[18:33], v[48:51], v[52:55], v[18:33]
	v_cmp_lt_f32_e32 vcc, s29, v72
	s_cbranch_vccz .LBB0_1668
	v_max_f32_e32 v36, v72, v72
	v_max_f32_e32 v37, 0, v36
	v_exp_f32_e64 v36, -v37
	v_add_f32_e32 v66, v66, v37
	v_mul_f32_e32 v34, v34, v36
	v_pk_mul_f32 v[114:115], v[114:115], v[36:37] op_sel_hi:[1,0]
	v_pk_mul_f32 v[112:113], v[112:113], v[36:37] op_sel_hi:[1,0]
	v_pk_mul_f32 v[110:111], v[110:111], v[36:37] op_sel_hi:[1,0]
	v_pk_mul_f32 v[108:109], v[108:109], v[36:37] op_sel_hi:[1,0]
	v_pk_mul_f32 v[106:107], v[106:107], v[36:37] op_sel_hi:[1,0]
	v_pk_mul_f32 v[104:105], v[104:105], v[36:37] op_sel_hi:[1,0]
	v_pk_mul_f32 v[102:103], v[102:103], v[36:37] op_sel_hi:[1,0]
	v_pk_mul_f32 v[100:101], v[100:101], v[36:37] op_sel_hi:[1,0]
	v_pk_mul_f32 v[32:33], v[36:37], v[32:33] op_sel_hi:[0,1]
	v_pk_mul_f32 v[30:31], v[36:37], v[30:31] op_sel_hi:[0,1]
	v_pk_mul_f32 v[28:29], v[36:37], v[28:29] op_sel_hi:[0,1]
	v_pk_mul_f32 v[26:27], v[36:37], v[26:27] op_sel_hi:[0,1]
	v_pk_mul_f32 v[24:25], v[36:37], v[24:25] op_sel_hi:[0,1]
	v_pk_mul_f32 v[22:23], v[36:37], v[22:23] op_sel_hi:[0,1]
	v_pk_mul_f32 v[20:21], v[36:37], v[20:21] op_sel_hi:[0,1]
	v_pk_mul_f32 v[18:19], v[36:37], v[18:19] op_sel_hi:[0,1]
	v_pk_mul_f32 v[16:17], v[36:37], v[16:17] op_sel_hi:[0,1]
	v_pk_mul_f32 v[14:15], v[36:37], v[14:15] op_sel_hi:[0,1]
	v_pk_mul_f32 v[12:13], v[36:37], v[12:13] op_sel_hi:[0,1]
	v_pk_mul_f32 v[10:11], v[36:37], v[10:11] op_sel_hi:[0,1]
	v_pk_mul_f32 v[8:9], v[36:37], v[8:9] op_sel_hi:[0,1]
	v_pk_mul_f32 v[6:7], v[36:37], v[6:7] op_sel_hi:[0,1]
	v_pk_mul_f32 v[4:5], v[36:37], v[4:5] op_sel_hi:[0,1]
	v_pk_mul_f32 v[2:3], v[36:37], v[2:3] op_sel_hi:[0,1]
